# attention second half-step: 7 v_exp_f32 of the previous tile moved in front of the first QK^T MFMA (into the LDS-read wait)
# baseline (speedup 1.0000x reference)
; __device__ __forceinline__ unsigned sel_bit_mask(unsigned w, int b) { unsigned m; asm("v_bfe_i32 %0, %1, %2, 1" : "=v"(m) : "v"(w), "n"(b)); return m; }
; template <bool SEL>
; __device__ __forceinline__ void partialSM(f32x16& p0, f32x16& p1, float& m_reg, float& mn, float& alpha, unsigned selw) {
;     ...
;     constexpr float C2 = 1.4426950408889634f * SCALE;
;     if (__builtin_expect(__all((pmax - m_reg) * SCALE <= THR), 1)) { mn = m_reg; alpha = 1.f; }
;     else { mn = fmaxf(m_reg, pmax); alpha = __builtin_amdgcn_exp2f((m_reg - mn) * C2); m_reg = mn; }
;     const float mnL = -mn * C2;
; #pragma unroll
;     for (int r = 0; r < 16; ++r) p0[r] = fmaf(p0[r], C2, mnL);
; #pragma unroll
;     for (int r = 0; r < 16; ++r) p1[r] = fmaf(p1[r], C2, mnL);
; #pragma unroll
;     for (int r = 0; r < 16; ++r) p0[r] = __builtin_amdgcn_exp2f(p0[r]);
;     if (SEL) {
; #pragma unroll
;         for (int r = 0; r < 16; ++r) p0[r] = __uint_as_float(__float_as_uint(p0[r]) & sel_bit_mask(selw, r));
;     }
; }
.LBB0_1816:
	v_cndmask_b32_e64 v197, v128, v184, s[2:3]
	v_mul_f32_e32 v172, 0xbe0293ee, v197
	v_fmamk_f32 v128, v96, 0x3e0293ee, v172
	v_fmamk_f32 v129, v97, 0x3e0293ee, v172
	v_fmamk_f32 v130, v98, 0x3e0293ee, v172
	v_fmamk_f32 v131, v99, 0x3e0293ee, v172
	v_fmamk_f32 v132, v100, 0x3e0293ee, v172
	v_fmamk_f32 v133, v101, 0x3e0293ee, v172
	v_fmamk_f32 v134, v102, 0x3e0293ee, v172
	v_fmamk_f32 v135, v103, 0x3e0293ee, v172
	v_fmamk_f32 v136, v104, 0x3e0293ee, v172
	v_fmamk_f32 v137, v105, 0x3e0293ee, v172
	v_fmamk_f32 v138, v106, 0x3e0293ee, v172
	v_fmamk_f32 v139, v107, 0x3e0293ee, v172
	v_fmamk_f32 v140, v108, 0x3e0293ee, v172
	v_fmamk_f32 v109, v109, 0x3e0293ee, v172
	v_fmamk_f32 v110, v110, 0x3e0293ee, v172
	v_fmamk_f32 v141, v111, 0x3e0293ee, v172
	v_fmamk_f32 v107, v80, 0x3e0293ee, v172
	v_fmamk_f32 v108, v81, 0x3e0293ee, v172
	v_fmamk_f32 v100, v82, 0x3e0293ee, v172
	v_fmamk_f32 v101, v83, 0x3e0293ee, v172
	v_fmamk_f32 v102, v84, 0x3e0293ee, v172
	v_fmamk_f32 v103, v85, 0x3e0293ee, v172
	v_fmamk_f32 v104, v86, 0x3e0293ee, v172
	v_fmamk_f32 v105, v87, 0x3e0293ee, v172
	v_fmamk_f32 v106, v88, 0x3e0293ee, v172
	v_fmamk_f32 v96, v89, 0x3e0293ee, v172
	v_fmamk_f32 v97, v90, 0x3e0293ee, v172
	v_fmamk_f32 v98, v91, 0x3e0293ee, v172
	v_fmamk_f32 v99, v92, 0x3e0293ee, v172
	v_exp_f32_e32 v80, v128
	v_exp_f32_e32 v81, v129
	v_exp_f32_e32 v82, v130
	v_exp_f32_e32 v83, v131
	v_exp_f32_e32 v84, v132
	v_exp_f32_e32 v85, v133
	v_exp_f32_e32 v86, v134
	v_exp_f32_e32 v87, v135
	v_exp_f32_e32 v88, v136
	v_exp_f32_e32 v89, v137
	v_exp_f32_e32 v90, v138
	v_exp_f32_e32 v91, v139
	v_exp_f32_e32 v92, v140
	v_exp_f32_e32 v128, v109
	v_exp_f32_e32 v111, v110
	v_exp_f32_e32 v129, v141
	v_fmamk_f32 v109, v93, 0x3e0293ee, v172
	v_fmamk_f32 v110, v94, 0x3e0293ee, v172
	v_fmac_f32_e32 v172, 0x3e0293ee, v95
	v_and_b32_e32 v81, v120, v81
	v_and_b32_e32 v80, v112, v80
	v_and_b32_e32 v83, v121, v83
	v_and_b32_e32 v82, v113, v82
	v_and_b32_e32 v85, v122, v85
	v_and_b32_e32 v84, v114, v84
	v_and_b32_e32 v87, v123, v87
	v_and_b32_e32 v86, v115, v86
	v_and_b32_e32 v89, v124, v89
	v_and_b32_e32 v88, v116, v88
	v_and_b32_e32 v91, v125, v91
	v_and_b32_e32 v90, v117, v90
	v_and_b32_e32 v93, v126, v128
	v_and_b32_e32 v92, v118, v92
	v_and_b32_e32 v95, v127, v129
	v_and_b32_e32 v94, v119, v111
	s_waitcnt lgkmcnt(0)
	s_barrier
; __device__ __forceinline__ unsigned sel_bit_mask(unsigned w, int b) { unsigned m; asm("v_bfe_i32 %0, %1, %2, 1" : "=v"(m) : "v"(w), "n"(b)); return m; }
; template <bool SEL>
; __device__ __forceinline__ void finishSM(f32x16& p0, f32x16& p1, float alpha, float& l_reg, bf16x8& pa0, bf16x8& pa1, bf16x8& pa2, bf16x8& pa3, unsigned selw) {
; #pragma unroll
;     for (int r = 0; r < 16; ++r) p1[r] = __builtin_amdgcn_exp2f(p1[r]);
;     if (SEL) {
; #pragma unroll
;         for (int r = 0; r < 16; ++r) p1[r] = __uint_as_float(__float_as_uint(p1[r]) & sel_bit_mask(selw, 16 + r));
;     }
;     float ps = 0;
; #pragma unroll
;     for (int r = 0; r < 16; ++r) ps += p0[r];
; #pragma unroll
;     for (int r = 0; r < 16; ++r) ps += p1[r];
;     { auto rr = __builtin_amdgcn_permlane32_swap(__float_as_uint(ps), __float_as_uint(ps), false, false);
;       ps = __uint_as_float(rr[0]) + __uint_as_float(rr[1]); }
;     l_reg = l_reg * alpha + ps;
;     ...
;     PK4(p0, 0, pa0); PK4(p0, 8, pa1); PK4(p1, 0, pa2); PK4(p1, 8, pa3);
;     ...
; }
; template <int KB, int QREG>
; __device__ __forceinline__ void qkt(f32x16& p0, f32x16& p1, const char* K_lds, int r32, int hi, const bf16x8* qr, const char* qlds) {
;     p0 = f32x16{}; p1 = f32x16{};
;     const char* kb[4];
; #pragma unroll
;     for (int dd = 0; dd < 4; ++dd) kb[dd] = K_lds + KB * SHM_K + KSWZ(r32, (dd * 16 + hi * 8) * 2);
; #pragma unroll
;     for (int d0 = 0; d0 < 8; ++d0) { const char* a = kb[d0 & 3] + (d0 >> 2) * 128;
;         bf16x8 b0 = *reinterpret_cast<const bf16x8*>(a);
;         bf16x8 b1 = *reinterpret_cast<const bf16x8*>(a + 32 * 256);
;         const bf16x8 qf = (d0 < QREG) ? qr[d0 < QREG ? d0 : 0] : *reinterpret_cast<const bf16x8*>(qlds + (d0 - QREG) * 1024);
;         p0 = __builtin_amdgcn_mfma_f32_32x32x16_bf16(b0, qf, p0, 0, 0, 0);
;         p1 = __builtin_amdgcn_mfma_f32_32x32x16_bf16(b1, qf, p1, 0, 0, 0); }
; }
	ds_read_b128 v[242:245], v208
	ds_read_b128 v[182:185], v208 offset:1024
	ds_read_b128 v[112:115], v213 offset:32768
	ds_read_b128 v[116:119], v213 offset:40960
	ds_read_b128 v[174:177], v212 offset:32768
	ds_read_b128 v[178:181], v212 offset:40960
	ds_read_b128 v[250:253], v211 offset:32768
	v_exp_f32_e32 v101, v101
	v_exp_f32_e32 v103, v103
	v_exp_f32_e32 v105, v105
	v_exp_f32_e32 v111, v96
	v_exp_f32_e32 v109, v109
	v_exp_f32_e32 v172, v172
	v_exp_f32_e32 v107, v107
	v_exp_f32_e32 v108, v108
	v_exp_f32_e32 v100, v100
	s_waitcnt lgkmcnt(4)
	v_mfma_f32_32x32x16_bf16 v[128:143], v[112:115], v[164:167], 0
	s_waitcnt lgkmcnt(3)
	v_mfma_f32_32x32x16_bf16 v[112:127], v[116:119], v[164:167], 0
	v_bfe_i32 v96, v217, 16, 1
	v_exp_f32_e32 v102, v102
	v_exp_f32_e32 v173, v97
	v_bfe_i32 v97, v217, 17, 1
	v_and_b32_e32 v96, v96, v107
	v_and_b32_e32 v97, v97, v108
	v_exp_f32_e32 v104, v104
	s_waitcnt lgkmcnt(2)
	v_mfma_f32_32x32x16_bf16 v[128:143], v[174:177], v[160:163], v[128:143]
	ds_read_b128 v[174:177], v211 offset:40960
	v_exp_f32_e32 v106, v106
	v_exp_f32_e32 v110, v110
	v_bfe_i32 v107, v217, 27, 1
	v_bfe_i32 v108, v217, 28, 1
	s_waitcnt lgkmcnt(2)
	v_mfma_f32_32x32x16_bf16 v[112:127], v[178:181], v[160:163], v[112:127]
	ds_read_b128 v[178:181], v210 offset:32768
	s_waitcnt lgkmcnt(2)
	v_mfma_f32_32x32x16_bf16 v[128:143], v[250:253], v[156:159], v[128:143]
	ds_read_b128 v[250:253], v210 offset:40960
	s_waitcnt lgkmcnt(2)
	v_mfma_f32_32x32x16_bf16 v[112:127], v[174:177], v[156:159], v[112:127]
	ds_read_b128 v[174:177], v213 offset:32896
	s_waitcnt lgkmcnt(2)
	v_mfma_f32_32x32x16_bf16 v[128:143], v[178:181], v[152:155], v[128:143]
	ds_read_b128 v[178:181], v213 offset:41088
	s_waitcnt lgkmcnt(2)
	v_mfma_f32_32x32x16_bf16 v[112:127], v[250:253], v[152:155], v[112:127]
	ds_read_b128 v[250:253], v212 offset:32896
	s_waitcnt lgkmcnt(2)
	v_mfma_f32_32x32x16_bf16 v[128:143], v[174:177], v[148:151], v[128:143]
	ds_read_b128 v[174:177], v212 offset:41088
	s_waitcnt lgkmcnt(2)
	v_mfma_f32_32x32x16_bf16 v[112:127], v[178:181], v[148:151], v[112:127]
	ds_read_b128 v[178:181], v211 offset:32896
	s_waitcnt lgkmcnt(2)
	v_mfma_f32_32x32x16_bf16 v[128:143], v[250:253], v[144:147], v[128:143]
	ds_read_b128 v[250:253], v211 offset:41088
	s_waitcnt lgkmcnt(2)
	v_mfma_f32_32x32x16_bf16 v[112:127], v[174:177], v[144:147], v[112:127]
	ds_read_b128 v[174:177], v210 offset:32896
	s_waitcnt lgkmcnt(2)
	v_mfma_f32_32x32x16_bf16 v[128:143], v[178:181], v[242:245], v[128:143]
	ds_read_b128 v[178:181], v210 offset:41088
	s_waitcnt lgkmcnt(2)
	v_mfma_f32_32x32x16_bf16 v[112:127], v[250:253], v[242:245], v[112:127]
	s_waitcnt lgkmcnt(1)
	v_mfma_f32_32x32x16_bf16 v[128:143], v[174:177], v[182:185], v[128:143]
	v_exp_f32_e32 v175, v99
	v_bfe_i32 v99, v217, 19, 1
	v_exp_f32_e32 v174, v98
	v_and_b32_e32 v99, v99, v101
	v_bfe_i32 v101, v217, 21, 1
	v_bfe_i32 v98, v217, 18, 1
	v_and_b32_e32 v107, v107, v174
	v_and_b32_e32 v101, v101, v103
	v_bfe_i32 v103, v217, 23, 1
	v_and_b32_e32 v98, v98, v100
	v_and_b32_e32 v103, v103, v105
	v_bfe_i32 v105, v217, 25, 1
	v_bfe_i32 v100, v217, 20, 1
	s_waitcnt lgkmcnt(0)
	v_mfma_f32_32x32x16_bf16 v[112:127], v[178:181], v[182:185], v[112:127]
	ds_read_b64_tr_b16 v[244:245], v206 offset:0x4000
	ds_read_b64_tr_b16 v[246:247], v206 offset:0x4800
	ds_read_b64_tr_b16 v[226:227], v206 offset:0x5000
	ds_read_b64_tr_b16 v[228:229], v206 offset:0x5800
	ds_read_b64_tr_b16 v[230:231], v206 offset:0x6000
	ds_read_b64_tr_b16 v[232:233], v206 offset:0x6800
	ds_read_b64_tr_b16 v[234:235], v206 offset:0x7000
	ds_read_b64_tr_b16 v[236:237], v206 offset:0x7800
	v_and_b32_e32 v105, v105, v111
	v_bfe_i32 v111, v217, 29, 1
	v_and_b32_e32 v100, v100, v102
	v_and_b32_e32 v109, v111, v109
	v_bfe_i32 v111, v217, 31, 1
	v_bfe_i32 v102, v217, 22, 1
	v_and_b32_e32 v108, v108, v175
	v_and_b32_e32 v111, v111, v172
	v_add_f32_e32 v172, 0, v80
	v_add_f32_e32 v172, v172, v81
	v_add_f32_e32 v172, v172, v82
	v_add_f32_e32 v172, v172, v83
	v_add_f32_e32 v172, v172, v84
	v_add_f32_e32 v172, v172, v85
	v_add_f32_e32 v172, v172, v86
	v_add_f32_e32 v172, v172, v87
	v_add_f32_e32 v172, v172, v88
	v_add_f32_e32 v172, v172, v89
	v_add_f32_e32 v172, v172, v90
	v_add_f32_e32 v172, v172, v91
	v_add_f32_e32 v172, v172, v92
	v_add_f32_e32 v172, v172, v93
	v_add_f32_e32 v172, v172, v94
	v_add_f32_e32 v172, v172, v95
	v_add_f32_e32 v172, v172, v96
	v_add_f32_e32 v172, v172, v97
	v_add_f32_e32 v172, v172, v98
	v_add_f32_e32 v172, v172, v99
	v_add_f32_e32 v172, v172, v100
	v_and_b32_e32 v102, v102, v104
	v_add_f32_e32 v172, v172, v101
	v_bfe_i32 v104, v217, 24, 1
	v_add_f32_e32 v172, v172, v102
	v_and_b32_e32 v104, v104, v106
	v_add_f32_e32 v172, v172, v103
	v_bfe_i32 v106, v217, 26, 1
	v_add_f32_e32 v172, v172, v104
	v_and_b32_e32 v106, v106, v173
	v_add_f32_e32 v172, v172, v105
	v_add_f32_e32 v172, v172, v106
	v_add_f32_e32 v172, v172, v107
	v_add_f32_e32 v172, v172, v108
	v_bfe_i32 v173, v217, 30, 1
	v_add_f32_e32 v172, v172, v109
	v_and_b32_e32 v110, v173, v110
	v_add_f32_e32 v172, v172, v110
	v_add_f32_e32 v220, v172, v111
	v_mov_b32_e32 v221, v220
	v_cvt_pk_bf16_f32 v172, v80, v81
	v_cvt_pk_bf16_f32 v173, v82, v83
	v_cvt_pk_bf16_f32 v174, v84, v85
	v_cvt_pk_bf16_f32 v175, v86, v87
	v_cvt_pk_bf16_f32 v176, v88, v89
	v_cvt_pk_bf16_f32 v177, v90, v91
	v_cvt_pk_bf16_f32 v178, v92, v93
	v_cvt_pk_bf16_f32 v179, v94, v95
	v_cvt_pk_bf16_f32 v180, v96, v97
	v_cvt_pk_bf16_f32 v181, v98, v99
	v_cvt_pk_bf16_f32 v182, v100, v101
	v_cvt_pk_bf16_f32 v183, v102, v103
	v_cvt_pk_bf16_f32 v184, v104, v105
	v_cvt_pk_bf16_f32 v185, v106, v107
	v_cvt_pk_bf16_f32 v186, v108, v109
	v_cvt_pk_bf16_f32 v187, v110, v111
	s_nop 1
	v_permlane32_swap_b32_e32 v220, v221
	v_permlane32_swap_b32_e32 v172, v174
	v_permlane32_swap_b32_e32 v173, v175
	v_permlane32_swap_b32_e32 v176, v178
	v_permlane32_swap_b32_e32 v177, v179
	v_permlane32_swap_b32_e32 v180, v182
	v_permlane32_swap_b32_e32 v181, v183
	v_permlane32_swap_b32_e32 v184, v186
	v_permlane32_swap_b32_e32 v185, v187
	v_mov_b32_e32 v195, v1
	v_lshl_add_u64 v[222:223], v[194:195], 2, s[44:45]
	global_load_dword v195, v[222:223], off
	s_add_i32 s2, s54, 1
	s_cmp_lt_i32 s2, s87
	s_cselect_b64 s[48:49], -1, 0
	s_cmp_ge_i32 s2, s87
	s_cbranch_scc1 .LBB0_1818
	v_add_u32_e32 v2, 64, v196
	v_add_u32_e32 v4, 0x60, v196
	v_ashrrev_i32_e32 v3, 31, v2
	v_ashrrev_i32_e32 v5, 31, v4
	v_lshlrev_b64 v[10:11], 10, v[2:3]
	v_lshlrev_b64 v[12:13], 10, v[4:5]
	v_lshl_add_u64 v[2:3], v[14:15], 0, v[10:11]
	v_lshl_add_u64 v[6:7], v[14:15], 0, v[12:13]
	v_lshl_add_u64 v[10:11], v[192:193], 0, v[10:11]
	v_lshl_add_u64 v[168:169], v[192:193], 0, v[12:13]
	global_load_dwordx4 v[2:5], v[2:3], off
	s_nop 0
	global_load_dwordx4 v[6:9], v[6:7], off
	s_nop 0
	global_load_dwordx4 v[10:13], v[10:11], off
	s_nop 0
	global_load_dwordx4 v[168:171], v[168:169], off
